# baseline (speedup 1.0000x reference)
.LBB0_2:
	s_or_b64 exec, exec, s[8:9]
	v_readfirstlane_b32 s36, v0
	v_lshlrev_b32_e32 v142, 6, v0
	s_cmp_lg_u32 s36, 0
	s_cbranch_scc1 .Lno_pf
	s_getpc_b64 s[38:39]
.Lpf_anchor:
	s_add_u32 s38, s38, 0xda8
	s_addc_u32 s39, s39, 0
	global_load_dword v142, v142, s[38:39]
.Lno_pf:
	v_lshlrev_b32_e32 v3, 3, v0
	v_and_b32_e32 v3, 0x7f8, v3
	s_waitcnt vmcnt(26)
	v_cvt_pk_bf16_f32 v85, v84, v85
	v_cvt_pk_bf16_f32 v84, v82, v83
	v_lshrrev_b32_e32 v82, 8, v0
	s_movk_i32 s16, 0x810
	s_waitcnt vmcnt(25)
	v_cvt_pk_bf16_f32 v81, v80, v81
	v_cvt_pk_bf16_f32 v80, v78, v79
	v_lshrrev_b32_e32 v78, 8, v122
	v_mad_u32_u24 v82, v82, s16, v3
	v_mad_u32_u24 v78, v78, s16, v3
	ds_write_b64 v82, v[84:85]
	ds_write_b64 v78, v[80:81]
	v_lshrrev_b32_e32 v80, 8, v123
	s_waitcnt vmcnt(24)
	v_cvt_pk_bf16_f32 v79, v92, v93
	v_cvt_pk_bf16_f32 v78, v90, v91
	v_mad_u32_u24 v80, v80, s16, v3
	ds_write_b64 v80, v[78:79]
	v_lshrrev_b32_e32 v80, 8, v124
	s_waitcnt vmcnt(23)
	v_cvt_pk_bf16_f32 v79, v88, v89
	v_cvt_pk_bf16_f32 v78, v86, v87
	v_mad_u32_u24 v80, v80, s16, v3
	ds_write_b64 v80, v[78:79]
	v_lshrrev_b32_e32 v80, 8, v125
	s_waitcnt vmcnt(22)
	v_cvt_pk_bf16_f32 v79, v100, v101
	v_cvt_pk_bf16_f32 v78, v98, v99
	v_mad_u32_u24 v80, v80, s16, v3
	ds_write_b64 v80, v[78:79]
	v_lshrrev_b32_e32 v80, 8, v130
	s_waitcnt vmcnt(21)
	v_cvt_pk_bf16_f32 v79, v96, v97
	v_cvt_pk_bf16_f32 v78, v94, v95
	v_mad_u32_u24 v80, v80, s16, v3
	ds_write_b64 v80, v[78:79]
	v_lshrrev_b32_e32 v80, 8, v131
	s_waitcnt vmcnt(20)
	v_cvt_pk_bf16_f32 v79, v108, v109
	v_cvt_pk_bf16_f32 v78, v106, v107
	v_mad_u32_u24 v80, v80, s16, v3
	ds_write_b64 v80, v[78:79]
	v_lshrrev_b32_e32 v80, 8, v134
	s_load_dwordx4 s[8:11], s[0:1], 0x20
	s_waitcnt vmcnt(19)
	v_cvt_pk_bf16_f32 v79, v104, v105
	v_cvt_pk_bf16_f32 v78, v102, v103
	v_mad_u32_u24 v80, v80, s16, v3
	ds_write_b64 v80, v[78:79]
	v_lshrrev_b32_e32 v80, 8, v135
	s_waitcnt vmcnt(18)
	v_cvt_pk_bf16_f32 v79, v120, v121
	v_cvt_pk_bf16_f32 v78, v118, v119
	v_mad_u32_u24 v80, v80, s16, v3
	ds_write_b64 v80, v[78:79]
	v_lshrrev_b32_e32 v80, 8, v136
	s_movk_i32 s14, 0x200
	s_waitcnt vmcnt(17)
	v_cvt_pk_bf16_f32 v79, v112, v113
	v_cvt_pk_bf16_f32 v78, v110, v111
	v_mad_u32_u24 v80, v80, s16, v3
	v_cmp_gt_u32_e32 vcc, s14, v0
	ds_write_b64 v80, v[78:79]
	s_and_saveexec_b64 s[14:15], vcc
	s_cbranch_execz .LBB0_4
	v_lshrrev_b32_e32 v80, 8, v137
	s_waitcnt vmcnt(16)
	v_cvt_pk_bf16_f32 v79, v116, v117
	v_cvt_pk_bf16_f32 v78, v114, v115
	v_mad_u32_u24 v3, v80, s16, v3
	ds_write_b64 v3, v[78:79]

	.amdhsa_kernel _Z14seg_sum_kernelPKfS0_S0_PDv8_DF16bS2_Pf
		.amdhsa_group_segment_fixed_size 141840
		.amdhsa_private_segment_fixed_size 0
		.amdhsa_kernarg_size 48
		.amdhsa_user_sgpr_count 2
		.amdhsa_user_sgpr_dispatch_ptr 0
		.amdhsa_user_sgpr_queue_ptr 0
		.amdhsa_user_sgpr_kernarg_segment_ptr 1
		.amdhsa_user_sgpr_dispatch_id 0
		.amdhsa_user_sgpr_kernarg_preload_length 0
		.amdhsa_user_sgpr_kernarg_preload_offset 0
		.amdhsa_user_sgpr_private_segment_size 0
		.amdhsa_uses_dynamic_stack 0
		.amdhsa_enable_private_segment 0
		.amdhsa_system_sgpr_workgroup_id_x 1
		.amdhsa_system_sgpr_workgroup_id_y 0
		.amdhsa_system_sgpr_workgroup_id_z 0
		.amdhsa_system_sgpr_workgroup_info 0
		.amdhsa_system_vgpr_workitem_id 0
		.amdhsa_next_free_vgpr 143
		.amdhsa_next_free_sgpr 96
		.amdhsa_accum_offset 144
		.amdhsa_reserve_vcc 1
		.amdhsa_float_round_mode_32 0
		.amdhsa_float_round_mode_16_64 0
		.amdhsa_float_denorm_mode_32 3
		.amdhsa_float_denorm_mode_16_64 3
		.amdhsa_dx10_clamp 1
		.amdhsa_ieee_mode 1
		.amdhsa_fp16_overflow 0
		.amdhsa_tg_split 0
		.amdhsa_exception_fp_ieee_invalid_op 0
		.amdhsa_exception_fp_denorm_src 0
		.amdhsa_exception_fp_ieee_div_zero 0
		.amdhsa_exception_fp_ieee_overflow 0
		.amdhsa_exception_fp_ieee_underflow 0
		.amdhsa_exception_fp_ieee_inexact 0
		.amdhsa_exception_int_div_zero 0
	.end_amdhsa_kernel

amdhsa.kernels:
  - .agpr_count:     0
    .args:
      - .actual_access:  read_only
        .address_space:  global
        .offset:         0
        .size:           8
        .value_kind:     global_buffer
      - .actual_access:  read_only
        .address_space:  global
        .offset:         8
        .size:           8
        .value_kind:     global_buffer
      - .actual_access:  read_only
        .address_space:  global
        .offset:         16
        .size:           8
        .value_kind:     global_buffer
      - .actual_access:  write_only
        .address_space:  global
        .offset:         24
        .size:           8
        .value_kind:     global_buffer
      - .actual_access:  write_only
        .address_space:  global
        .offset:         32
        .size:           8
        .value_kind:     global_buffer
      - .actual_access:  write_only
        .address_space:  global
        .offset:         40
        .size:           8
        .value_kind:     global_buffer
    .group_segment_fixed_size: 141840
    .kernarg_segment_align: 8
    .kernarg_segment_size: 48
    .language:       OpenCL C
    .language_version:
      - 2
      - 0
    .max_flat_workgroup_size: 768
    .name:           _Z14seg_sum_kernelPKfS0_S0_PDv8_DF16bS2_Pf
    .private_segment_fixed_size: 0
    .sgpr_count:     42
    .sgpr_spill_count: 0
    .symbol:         _Z14seg_sum_kernelPKfS0_S0_PDv8_DF16bS2_Pf.kd
    .uniform_work_group_size: 1
    .uses_dynamic_stack: false
    .vgpr_count:     143
    .vgpr_spill_count: 0
    .wavefront_size: 64
  - .agpr_count:     16
    .args:
      - .actual_access:  read_only
        .address_space:  global
        .offset:         0
        .size:           8
        .value_kind:     global_buffer
      - .actual_access:  read_only
        .address_space:  global
        .offset:         8
        .size:           8
        .value_kind:     global_buffer
      - .actual_access:  read_only
        .address_space:  global
        .offset:         16
        .size:           8
        .value_kind:     global_buffer
      - .actual_access:  read_only
        .address_space:  global
        .offset:         24
        .size:           8
        .value_kind:     global_buffer
      - .actual_access:  write_only
        .address_space:  global
        .offset:         32
        .size:           8
        .value_kind:     global_buffer
      - .actual_access:  write_only
        .address_space:  global
        .offset:         40
        .size:           8
        .value_kind:     global_buffer
      - .actual_access:  write_only
        .address_space:  global
        .offset:         48
        .size:           8
        .value_kind:     global_buffer
    .group_segment_fixed_size: 17152
    .kernarg_segment_align: 8
    .kernarg_segment_size: 56
    .language:       OpenCL C
    .language_version:
      - 2
      - 0
    .max_flat_workgroup_size: 256
    .name:           _Z13logits_kernelPKDv8_DF16bS1_PKfS3_PDv2_fS5_Pf
    .private_segment_fixed_size: 0
    .sgpr_count:     37
    .sgpr_spill_count: 0
    .symbol:         _Z13logits_kernelPKDv8_DF16bS1_PKfS3_PDv2_fS5_Pf.kd
    .uniform_work_group_size: 1
    .uses_dynamic_stack: false
    .vgpr_count:     268
    .vgpr_spill_count: 0
    .wavefront_size: 64
  - .agpr_count:     0
    .args:
      - .actual_access:  read_only
        .address_space:  global
        .offset:         0
        .size:           8
        .value_kind:     global_buffer
      - .actual_access:  read_only
        .address_space:  global
        .offset:         8
        .size:           8
        .value_kind:     global_buffer
      - .actual_access:  read_only
        .address_space:  global
        .offset:         16
        .size:           8
        .value_kind:     global_buffer
      - .actual_access:  read_only
        .address_space:  global
        .offset:         24
        .size:           8
        .value_kind:     global_buffer
      - .actual_access:  write_only
        .address_space:  global
        .offset:         32
        .size:           8
        .value_kind:     global_buffer
    .group_segment_fixed_size: 128
    .kernarg_segment_align: 8
    .kernarg_segment_size: 40
    .language:       OpenCL C
    .language_version:
      - 2
      - 0
    .max_flat_workgroup_size: 1024
    .name:           _Z12final_kernelPKDv4_fS1_PKfS3_Pf
    .private_segment_fixed_size: 0
    .sgpr_count:     20
    .sgpr_spill_count: 0
    .symbol:         _Z12final_kernelPKDv4_fS1_PKfS3_Pf.kd
    .uniform_work_group_size: 1
    .uses_dynamic_stack: false
    .vgpr_count:     52
    .vgpr_spill_count: 0
    .wavefront_size: 64
